# baseline (speedup 1.0000x reference)
_Z16sum_layer_kernelPKfS0_Pf:
	s_load_dwordx4 s[4:7], s[0:1], 0x0
	s_load_dwordx2 s[8:9], s[0:1], 0x10
	v_lshrrev_b32_e32 v42, 6, v0
	v_bfe_u32 v41, v0, 5, 1
	v_and_b32_e32 v40, 31, v0
	v_readfirstlane_b32 s23, v42
	v_and_b32_e32 v43, 7, v0
	v_bfe_u32 v44, v0, 3, 3
	s_lshl_b32 s3, s2, 12
	s_lshr_b32 s40, s23, 1
	s_lshr_b32 s41, s2, 8
	s_cmp_lg_u32 s40, s41
	s_cbranch_scc1 .Lexit_idle_wave
	s_and_b32 s23, s23, 1
	v_and_b32_e32 v42, 1, v42
	s_lshl_b32 s19, s2, 7
	s_lshl_b32 s54, s23, 12
	s_add_u32 s54, s54, 0x4000
	s_lshl_b32 s23, s23, 13
	s_add_u32 s52, s23, 0x1000
	v_lshlrev_b32_e32 v1, 11, v41
	v_lshl_or_b32 v1, v40, 2, v1
	v_lshrrev_b32_e32 v46, 1, v44
	v_xor_b32_e32 v46, v43, v46
	v_lshlrev_b32_e32 v46, 4, v46
	v_lshl_add_u32 v35, v44, 16, v46
	v_lshl_add_u32 v35, v42, 22, v35
	v_add_u32_e32 v35, s19, v35
	v_xor_b32_e32 v86, 64, v35
	v_and_b32_e32 v45, 63, v0
	v_lshlrev_b32_e32 v37, 4, v45
	s_mov_b32 s20, 0x7fc00
	s_mov_b32 s21, 0xff800
	s_mov_b32 s22, 0x17f400
	s_mov_b32 s48, 0x200000
	s_mov_b32 s49, 0x27fc00
	s_mov_b32 s50, 0x2ff800
	s_mov_b32 s51, 0x37f400
	s_mov_b32 s14, 0x200000
	s_mov_b32 s15, 0x20000
	s_waitcnt lgkmcnt(0)
	s_mov_b32 s12, s6
	s_and_b32 s13, s7, 0xffff
	s_and_b32 s5, s5, 0xffff
	s_mov_b32 s6, 0x800000
	s_mov_b32 s7, s15
	s_mov_b32 m0, s54
	s_nop 0
	buffer_load_dwordx4 v37, s[12:15], s3 offen nt lds
	buffer_load_dwordx4 v37, s[12:15], s3 offen offset:1024 nt lds
	buffer_load_dwordx4 v37, s[12:15], s3 offen offset:2048 nt lds
	buffer_load_dwordx4 v37, s[12:15], s3 offen offset:3072 nt lds
	s_mov_b32 m0, s23
	s_nop 0
	buffer_load_dwordx4 v35, s[4:7], 0 offen nt lds
	buffer_load_dwordx4 v86, s[4:7], s20 offen offset:1024 nt lds
	buffer_load_dwordx4 v35, s[4:7], s21 offen offset:2048 nt lds
	buffer_load_dwordx4 v86, s[4:7], s22 offen offset:3072 nt lds
	s_mov_b32 m0, s52
	s_nop 0
	buffer_load_dwordx4 v35, s[4:7], s48 offen nt lds
	buffer_load_dwordx4 v86, s[4:7], s49 offen offset:1024 nt lds
	buffer_load_dwordx4 v35, s[4:7], s50 offen offset:2048 nt lds
	buffer_load_dwordx4 v86, s[4:7], s51 offen offset:3072 nt lds
	v_lshlrev_b32_e32 v36, 2, v40
	v_lshl_add_u32 v36, v41, 18, v36
	v_lshl_add_u32 v36, v42, 22, v36
	v_add_u32_e32 v36, s19, v36
	v_add_u32_e32 v87, 0x200000, v36
	v_bfe_u32 v47, v40, 1, 3
	v_lshlrev_b32_e32 v39, 2, v41
	v_xor_b32_e32 v39, v39, v47
	v_lshlrev_b32_e32 v39, 4, v39
	v_lshl_add_u32 v39, v40, 7, v39
	v_lshl_add_u32 v39, v42, 13, v39
	v_xor_b32_e32 v81, 16, v39
	v_xor_b32_e32 v82, 32, v39
	v_xor_b32_e32 v83, 48, v39
	v_cmp_gt_u32_e32 vcc, 32, v45
	v_mov_b32_e32 v34, 0xc1600000
	v_mov_b32_e32 v84, 0x3fb8aa3b
	v_mov_b32_e32 v85, 0x3f317218
	s_lshl_b32 s24, 1, 16
	s_lshl_b32 s25, 2, 16
	s_lshl_b32 s26, 3, 16
	s_lshl_b32 s27, 8, 16
	s_lshl_b32 s28, 9, 16
	s_lshl_b32 s29, 10, 16
	s_lshl_b32 s30, 11, 16
	s_lshl_b32 s31, 16, 16
	s_lshl_b32 s32, 17, 16
	s_lshl_b32 s33, 18, 16
	s_lshl_b32 s34, 19, 16
	s_lshl_b32 s35, 24, 16
	s_lshl_b32 s36, 25, 16
	s_lshl_b32 s37, 26, 16
	s_lshl_b32 s38, 27, 16
	s_and_b32 s9, s9, 0xffff
	s_mov_b32 s10, s6
	s_mov_b32 s11, s15
	v_lshl_add_u32 v38, v42, 12, v1
	v_add_u32_e32 v38, 0x4000, v38
	v_add_u32_e32 v80, 0x400, v38
	s_waitcnt vmcnt(8)
	ds_read2_b32 v[18:19], v38 offset0:0 offset1:32
	ds_read2_b32 v[20:21], v38 offset0:64 offset1:96
	ds_read2_b32 v[22:23], v38 offset0:128 offset1:160
	ds_read2_b32 v[24:25], v38 offset0:192 offset1:224
	ds_read2_b32 v[26:27], v80 offset0:0 offset1:32
	ds_read2_b32 v[28:29], v80 offset0:64 offset1:96
	ds_read2_b32 v[30:31], v80 offset0:128 offset1:160
	ds_read2_b32 v[32:33], v80 offset0:192 offset1:224
	s_waitcnt lgkmcnt(0)
	v_max3_f32 v48, v18, v19, v20
	v_max3_f32 v50, v21, v22, v23
	v_max3_f32 v48, v48, v24, v25
	v_max3_f32 v50, v50, v26, v27
	v_max3_f32 v48, v48, v28, v29
	v_max3_f32 v50, v50, v30, v31
	v_max3_f32 v48, v48, v32, v33
	v_max_f32_e32 v48, v48, v50
	v_mov_b32_e32 v50, v48
	s_nop 1
	v_permlane32_swap_b32_e32 v48, v50
	v_max_f32_e32 v48, v48, v50
	v_fmamk_f32 v48, v48, 0x3fb8aa3b, v34
	v_pk_fma_f32 v[18:19], v[18:19], v[84:85], v[48:49] op_sel_hi:[1,0,0] neg_lo:[0,0,1] neg_hi:[0,0,1]
	v_exp_f32_e32 v18, v18
	v_exp_f32_e32 v19, v19
	v_pk_fma_f32 v[20:21], v[20:21], v[84:85], v[48:49] op_sel_hi:[1,0,0] neg_lo:[0,0,1] neg_hi:[0,0,1]
	v_exp_f32_e32 v20, v20
	v_exp_f32_e32 v21, v21
	v_pk_fma_f32 v[22:23], v[22:23], v[84:85], v[48:49] op_sel_hi:[1,0,0] neg_lo:[0,0,1] neg_hi:[0,0,1]
	v_exp_f32_e32 v22, v22
	v_exp_f32_e32 v23, v23
	v_pk_fma_f32 v[24:25], v[24:25], v[84:85], v[48:49] op_sel_hi:[1,0,0] neg_lo:[0,0,1] neg_hi:[0,0,1]
	v_exp_f32_e32 v24, v24
	v_exp_f32_e32 v25, v25
	v_pk_fma_f32 v[26:27], v[26:27], v[84:85], v[48:49] op_sel_hi:[1,0,0] neg_lo:[0,0,1] neg_hi:[0,0,1]
	v_exp_f32_e32 v26, v26
	v_exp_f32_e32 v27, v27
	v_pk_fma_f32 v[28:29], v[28:29], v[84:85], v[48:49] op_sel_hi:[1,0,0] neg_lo:[0,0,1] neg_hi:[0,0,1]
	v_exp_f32_e32 v28, v28
	v_exp_f32_e32 v29, v29
	v_pk_fma_f32 v[30:31], v[30:31], v[84:85], v[48:49] op_sel_hi:[1,0,0] neg_lo:[0,0,1] neg_hi:[0,0,1]
	v_exp_f32_e32 v30, v30
	v_exp_f32_e32 v31, v31
	v_pk_fma_f32 v[32:33], v[32:33], v[84:85], v[48:49] op_sel_hi:[1,0,0] neg_lo:[0,0,1] neg_hi:[0,0,1]
	v_exp_f32_e32 v32, v32
	v_exp_f32_e32 v33, v33
	v_pk_add_f32 v[56:57], v[18:19], v[20:21]
	v_pk_add_f32 v[58:59], v[22:23], v[24:25]
	v_pk_add_f32 v[60:61], v[26:27], v[28:29]
	v_pk_add_f32 v[62:63], v[30:31], v[32:33]
	v_pk_add_f32 v[56:57], v[56:57], v[58:59]
	v_pk_add_f32 v[60:61], v[60:61], v[62:63]
	v_pk_add_f32 v[56:57], v[56:57], v[60:61]
	v_add_f32_e32 v50, v56, v57
	v_mov_b32_e32 v51, v50
	s_nop 1
	v_permlane32_swap_b32_e32 v50, v51
	v_add_f32_e32 v50, v50, v51
	v_log_f32_e32 v50, v50
	v_cvt_pk_f16_f32 v40, v18, v19
	v_cvt_pk_f16_f32 v41, v20, v21
	v_cvt_pk_f16_f32 v42, v22, v23
	v_cvt_pk_f16_f32 v43, v24, v25
	v_cvt_pk_f16_f32 v44, v26, v27
	v_cvt_pk_f16_f32 v45, v28, v29
	v_cvt_pk_f16_f32 v46, v30, v31
	v_cvt_pk_f16_f32 v47, v32, v33
	v_add_f32_e32 v50, 0x41600000, v50
	v_mul_f32_e32 v50, 0xbf317218, v50
	v_cndmask_b32_e64 v51, v50, 1.0, vcc
	s_waitcnt vmcnt(4)
	ds_read_b128 v[2:5], v39
	ds_read_b128 v[6:9], v81
	ds_read_b128 v[10:13], v82
	ds_read_b128 v[14:17], v83
	s_waitcnt lgkmcnt(2)
	v_max3_f32 v52, v2, v3, v4
	v_max3_f32 v53, v5, v6, v7
	v_max_f32_e32 v52, v52, v8
	v_max_f32_e32 v53, v53, v9
	s_waitcnt lgkmcnt(0)
	v_max3_f32 v52, v52, v10, v11
	v_max3_f32 v53, v53, v12, v13
	v_max3_f32 v52, v52, v14, v15
	v_max3_f32 v53, v53, v16, v17
	v_max_f32_e32 v52, v52, v53
	v_mov_b32_e32 v53, v52
	s_nop 1
	v_permlane32_swap_b32_e32 v52, v53
	v_max_f32_e32 v52, v52, v53
	v_cndmask_b32_e32 v54, 1.0, v52, vcc
	v_fmamk_f32 v48, v52, 0x3fb8aa3b, v34
	v_pk_fma_f32 v[2:3], v[2:3], v[84:85], v[48:49] op_sel_hi:[1,0,0] neg_lo:[0,0,1] neg_hi:[0,0,1]
	v_mfma_f32_32x32x2_f32 v[64:79], v54, v51, 0
	v_exp_f32_e32 v2, v2
	v_exp_f32_e32 v3, v3
	v_pk_fma_f32 v[4:5], v[4:5], v[84:85], v[48:49] op_sel_hi:[1,0,0] neg_lo:[0,0,1] neg_hi:[0,0,1]
	v_exp_f32_e32 v4, v4
	v_exp_f32_e32 v5, v5
	v_pk_fma_f32 v[6:7], v[6:7], v[84:85], v[48:49] op_sel_hi:[1,0,0] neg_lo:[0,0,1] neg_hi:[0,0,1]
	v_exp_f32_e32 v6, v6
	v_exp_f32_e32 v7, v7
	v_pk_fma_f32 v[8:9], v[8:9], v[84:85], v[48:49] op_sel_hi:[1,0,0] neg_lo:[0,0,1] neg_hi:[0,0,1]
	v_exp_f32_e32 v8, v8
	v_exp_f32_e32 v9, v9
	v_pk_fma_f32 v[10:11], v[10:11], v[84:85], v[48:49] op_sel_hi:[1,0,0] neg_lo:[0,0,1] neg_hi:[0,0,1]
	v_exp_f32_e32 v10, v10
	v_cvt_pk_f16_f32 v56, v2, v3
	v_cvt_pk_f16_f32 v57, v4, v5
	v_cvt_pk_f16_f32 v58, v6, v7
	v_cvt_pk_f16_f32 v59, v8, v9
	v_exp_f32_e32 v11, v11
	v_pk_fma_f32 v[12:13], v[12:13], v[84:85], v[48:49] op_sel_hi:[1,0,0] neg_lo:[0,0,1] neg_hi:[0,0,1]
	v_exp_f32_e32 v12, v12
	v_mfma_f32_32x32x16_f16 v[18:33], v[56:59], v[40:43], 0
	v_exp_f32_e32 v13, v13
	v_pk_fma_f32 v[14:15], v[14:15], v[84:85], v[48:49] op_sel_hi:[1,0,0] neg_lo:[0,0,1] neg_hi:[0,0,1]
	v_exp_f32_e32 v14, v14
	v_exp_f32_e32 v15, v15
	v_pk_fma_f32 v[16:17], v[16:17], v[84:85], v[48:49] op_sel_hi:[1,0,0] neg_lo:[0,0,1] neg_hi:[0,0,1]
	v_exp_f32_e32 v16, v16
	v_exp_f32_e32 v17, v17
	v_cvt_pk_f16_f32 v60, v10, v11
	v_cvt_pk_f16_f32 v61, v12, v13
	v_cvt_pk_f16_f32 v62, v14, v15
	v_cvt_pk_f16_f32 v63, v16, v17
	s_nop 1
	v_mfma_f32_32x32x16_f16 v[18:33], v[60:63], v[44:47], v[18:33]
	s_nop 11
	v_log_f32_e32 v18, v18
	v_log_f32_e32 v19, v19
	v_log_f32_e32 v20, v20
	v_log_f32_e32 v21, v21
	v_log_f32_e32 v22, v22
	v_log_f32_e32 v23, v23
	v_pk_fma_f32 v[64:65], v[18:19], v[84:85], v[64:65] op_sel:[0,1,0] op_sel_hi:[1,1,1]
	buffer_store_dword v64, v36, s[8:11], 0 offen
	buffer_store_dword v65, v36, s[8:11], s24 offen
	v_log_f32_e32 v24, v24
	v_log_f32_e32 v25, v25
	v_pk_fma_f32 v[66:67], v[20:21], v[84:85], v[66:67] op_sel:[0,1,0] op_sel_hi:[1,1,1]
	buffer_store_dword v66, v36, s[8:11], s25 offen
	buffer_store_dword v67, v36, s[8:11], s26 offen
	v_log_f32_e32 v26, v26
	v_log_f32_e32 v27, v27
	v_pk_fma_f32 v[68:69], v[22:23], v[84:85], v[68:69] op_sel:[0,1,0] op_sel_hi:[1,1,1]
	buffer_store_dword v68, v36, s[8:11], s27 offen
	buffer_store_dword v69, v36, s[8:11], s28 offen
	v_log_f32_e32 v28, v28
	v_log_f32_e32 v29, v29
	v_pk_fma_f32 v[70:71], v[24:25], v[84:85], v[70:71] op_sel:[0,1,0] op_sel_hi:[1,1,1]
	buffer_store_dword v70, v36, s[8:11], s29 offen
	buffer_store_dword v71, v36, s[8:11], s30 offen
	v_log_f32_e32 v30, v30
	v_log_f32_e32 v31, v31
	v_pk_fma_f32 v[72:73], v[26:27], v[84:85], v[72:73] op_sel:[0,1,0] op_sel_hi:[1,1,1]
	buffer_store_dword v72, v36, s[8:11], s31 offen
	buffer_store_dword v73, v36, s[8:11], s32 offen
	v_log_f32_e32 v32, v32
	v_log_f32_e32 v33, v33
	v_pk_fma_f32 v[74:75], v[28:29], v[84:85], v[74:75] op_sel:[0,1,0] op_sel_hi:[1,1,1]
	buffer_store_dword v74, v36, s[8:11], s33 offen
	buffer_store_dword v75, v36, s[8:11], s34 offen
	v_pk_fma_f32 v[76:77], v[30:31], v[84:85], v[76:77] op_sel:[0,1,0] op_sel_hi:[1,1,1]
	buffer_store_dword v76, v36, s[8:11], s35 offen
	buffer_store_dword v77, v36, s[8:11], s36 offen
	v_pk_fma_f32 v[78:79], v[32:33], v[84:85], v[78:79] op_sel:[0,1,0] op_sel_hi:[1,1,1]
	buffer_store_dword v78, v36, s[8:11], s37 offen
	buffer_store_dword v79, v36, s[8:11], s38 offen
	s_waitcnt vmcnt(16)
	ds_read_b128 v[2:5], v39 offset:4096
	ds_read_b128 v[6:9], v81 offset:4096
	ds_read_b128 v[10:13], v82 offset:4096
	ds_read_b128 v[14:17], v83 offset:4096
	s_waitcnt lgkmcnt(2)
	v_max3_f32 v52, v2, v3, v4
	v_max3_f32 v53, v5, v6, v7
	v_max_f32_e32 v52, v52, v8
	v_max_f32_e32 v53, v53, v9
	s_waitcnt lgkmcnt(0)
	v_max3_f32 v52, v52, v10, v11
	v_max3_f32 v53, v53, v12, v13
	v_max3_f32 v52, v52, v14, v15
	v_max3_f32 v53, v53, v16, v17
	v_max_f32_e32 v52, v52, v53
	v_mov_b32_e32 v53, v52
	s_nop 1
	v_permlane32_swap_b32_e32 v52, v53
	v_max_f32_e32 v52, v52, v53
	v_cndmask_b32_e32 v54, 1.0, v52, vcc
	v_fmamk_f32 v48, v52, 0x3fb8aa3b, v34
	v_pk_fma_f32 v[2:3], v[2:3], v[84:85], v[48:49] op_sel_hi:[1,0,0] neg_lo:[0,0,1] neg_hi:[0,0,1]
	v_mfma_f32_32x32x2_f32 v[88:103], v54, v51, 0
	v_exp_f32_e32 v2, v2
	v_exp_f32_e32 v3, v3
	v_pk_fma_f32 v[4:5], v[4:5], v[84:85], v[48:49] op_sel_hi:[1,0,0] neg_lo:[0,0,1] neg_hi:[0,0,1]
	v_exp_f32_e32 v4, v4
	v_exp_f32_e32 v5, v5
	v_pk_fma_f32 v[6:7], v[6:7], v[84:85], v[48:49] op_sel_hi:[1,0,0] neg_lo:[0,0,1] neg_hi:[0,0,1]
	v_exp_f32_e32 v6, v6
	v_exp_f32_e32 v7, v7
	v_pk_fma_f32 v[8:9], v[8:9], v[84:85], v[48:49] op_sel_hi:[1,0,0] neg_lo:[0,0,1] neg_hi:[0,0,1]
	v_exp_f32_e32 v8, v8
	v_exp_f32_e32 v9, v9
	v_pk_fma_f32 v[10:11], v[10:11], v[84:85], v[48:49] op_sel_hi:[1,0,0] neg_lo:[0,0,1] neg_hi:[0,0,1]
	v_exp_f32_e32 v10, v10
	v_cvt_pk_f16_f32 v56, v2, v3
	v_cvt_pk_f16_f32 v57, v4, v5
	v_cvt_pk_f16_f32 v58, v6, v7
	v_cvt_pk_f16_f32 v59, v8, v9
	v_exp_f32_e32 v11, v11
	v_pk_fma_f32 v[12:13], v[12:13], v[84:85], v[48:49] op_sel_hi:[1,0,0] neg_lo:[0,0,1] neg_hi:[0,0,1]
	v_exp_f32_e32 v12, v12
	v_mfma_f32_32x32x16_f16 v[18:33], v[56:59], v[40:43], 0
	v_exp_f32_e32 v13, v13
	v_pk_fma_f32 v[14:15], v[14:15], v[84:85], v[48:49] op_sel_hi:[1,0,0] neg_lo:[0,0,1] neg_hi:[0,0,1]
	v_exp_f32_e32 v14, v14
	v_exp_f32_e32 v15, v15
	v_pk_fma_f32 v[16:17], v[16:17], v[84:85], v[48:49] op_sel_hi:[1,0,0] neg_lo:[0,0,1] neg_hi:[0,0,1]
	v_exp_f32_e32 v16, v16
	v_exp_f32_e32 v17, v17
	v_cvt_pk_f16_f32 v60, v10, v11
	v_cvt_pk_f16_f32 v61, v12, v13
	v_cvt_pk_f16_f32 v62, v14, v15
	v_cvt_pk_f16_f32 v63, v16, v17
	s_nop 1
	v_mfma_f32_32x32x16_f16 v[18:33], v[60:63], v[44:47], v[18:33]
	s_nop 11
	v_log_f32_e32 v18, v18
	v_log_f32_e32 v19, v19
	v_log_f32_e32 v20, v20
	v_log_f32_e32 v21, v21
	v_log_f32_e32 v22, v22
	v_log_f32_e32 v23, v23
	v_pk_fma_f32 v[88:89], v[18:19], v[84:85], v[88:89] op_sel:[0,1,0] op_sel_hi:[1,1,1]
	buffer_store_dword v88, v87, s[8:11], 0 offen
	buffer_store_dword v89, v87, s[8:11], s24 offen
	v_log_f32_e32 v24, v24
	v_log_f32_e32 v25, v25
	v_pk_fma_f32 v[90:91], v[20:21], v[84:85], v[90:91] op_sel:[0,1,0] op_sel_hi:[1,1,1]
	buffer_store_dword v90, v87, s[8:11], s25 offen
	buffer_store_dword v91, v87, s[8:11], s26 offen
	v_log_f32_e32 v26, v26
	v_log_f32_e32 v27, v27
	v_pk_fma_f32 v[92:93], v[22:23], v[84:85], v[92:93] op_sel:[0,1,0] op_sel_hi:[1,1,1]
	buffer_store_dword v92, v87, s[8:11], s27 offen
	buffer_store_dword v93, v87, s[8:11], s28 offen
	v_log_f32_e32 v28, v28
	v_log_f32_e32 v29, v29
	v_pk_fma_f32 v[94:95], v[24:25], v[84:85], v[94:95] op_sel:[0,1,0] op_sel_hi:[1,1,1]
	buffer_store_dword v94, v87, s[8:11], s29 offen
	buffer_store_dword v95, v87, s[8:11], s30 offen
	v_log_f32_e32 v30, v30
	v_log_f32_e32 v31, v31
	v_pk_fma_f32 v[96:97], v[26:27], v[84:85], v[96:97] op_sel:[0,1,0] op_sel_hi:[1,1,1]
	buffer_store_dword v96, v87, s[8:11], s31 offen
	buffer_store_dword v97, v87, s[8:11], s32 offen
	v_log_f32_e32 v32, v32
	v_log_f32_e32 v33, v33
	v_pk_fma_f32 v[98:99], v[28:29], v[84:85], v[98:99] op_sel:[0,1,0] op_sel_hi:[1,1,1]
	buffer_store_dword v98, v87, s[8:11], s33 offen
	buffer_store_dword v99, v87, s[8:11], s34 offen
	v_pk_fma_f32 v[100:101], v[30:31], v[84:85], v[100:101] op_sel:[0,1,0] op_sel_hi:[1,1,1]
	buffer_store_dword v100, v87, s[8:11], s35 offen
	buffer_store_dword v101, v87, s[8:11], s36 offen
	v_pk_fma_f32 v[102:103], v[32:33], v[84:85], v[102:103] op_sel:[0,1,0] op_sel_hi:[1,1,1]
	buffer_store_dword v102, v87, s[8:11], s37 offen
	buffer_store_dword v103, v87, s[8:11], s38 offen
.Lexit_idle_wave:
	s_waitcnt lgkmcnt(0)
	s_endpgm

	.amdhsa_kernel _Z16sum_layer_kernelPKfS0_Pf
		.amdhsa_group_segment_fixed_size 24576
		.amdhsa_private_segment_fixed_size 0
		.amdhsa_kernarg_size 24
		.amdhsa_user_sgpr_count 2
		.amdhsa_user_sgpr_dispatch_ptr 0
		.amdhsa_user_sgpr_queue_ptr 0
		.amdhsa_user_sgpr_kernarg_segment_ptr 1
		.amdhsa_user_sgpr_dispatch_id 0
		.amdhsa_user_sgpr_kernarg_preload_length 0
		.amdhsa_user_sgpr_kernarg_preload_offset 0
		.amdhsa_user_sgpr_private_segment_size 0
		.amdhsa_uses_dynamic_stack 0
		.amdhsa_enable_private_segment 0
		.amdhsa_system_sgpr_workgroup_id_x 1
		.amdhsa_system_sgpr_workgroup_id_y 0
		.amdhsa_system_sgpr_workgroup_id_z 0
		.amdhsa_system_sgpr_workgroup_info 0
		.amdhsa_system_vgpr_workitem_id 0
		.amdhsa_next_free_vgpr 104
		.amdhsa_next_free_sgpr 56
		.amdhsa_accum_offset 104
		.amdhsa_reserve_vcc 1
		.amdhsa_float_round_mode_32 0
		.amdhsa_float_round_mode_16_64 0
		.amdhsa_float_denorm_mode_32 3
		.amdhsa_float_denorm_mode_16_64 3
		.amdhsa_dx10_clamp 1
		.amdhsa_ieee_mode 1
		.amdhsa_fp16_overflow 0
		.amdhsa_tg_split 0
		.amdhsa_exception_fp_ieee_invalid_op 0
		.amdhsa_exception_fp_denorm_src 0
		.amdhsa_exception_fp_ieee_div_zero 0
		.amdhsa_exception_fp_ieee_overflow 0
		.amdhsa_exception_fp_ieee_underflow 0
		.amdhsa_exception_fp_ieee_inexact 0
		.amdhsa_exception_int_div_zero 0
	.end_amdhsa_kernel

amdhsa.kernels:
  - .agpr_count:     0
    .args:
      - .address_space:  global
        .offset:         0
        .size:           8
        .value_kind:     global_buffer
      - .address_space:  global
        .offset:         8
        .size:           8
        .value_kind:     global_buffer
      - .address_space:  global
        .offset:         16
        .size:           8
        .value_kind:     global_buffer
    .group_segment_fixed_size: 24576
    .kernarg_segment_align: 8
    .kernarg_segment_size: 24
    .language:       OpenCL C
    .language_version:
      - 2
      - 0
    .max_flat_workgroup_size: 256
    .name:           _Z16sum_layer_kernelPKfS0_Pf
    .private_segment_fixed_size: 0
    .sgpr_count:     62
    .sgpr_spill_count: 0
    .symbol:         _Z16sum_layer_kernelPKfS0_Pf.kd
    .uniform_work_group_size: 1
    .uses_dynamic_stack: false
    .vgpr_count:     104
    .vgpr_spill_count: 0
    .wavefront_size: 64
